# speedup vs baseline: 1.0108x; 1.0043x over previous
_Z13reduce_kernelPKDF16_Pf:
	s_load_dwordx4 s[4:7], s[0:1], 0x0
	v_lshl_or_b32 v2, s2, 8, v0
	v_lshlrev_b32_e32 v1, 3, v2
	v_mov_b32_e32 v6, 0
	v_mov_b32_e32 v7, 0
	v_mov_b32_e32 v8, 0
	v_mov_b32_e32 v9, 0
	v_add_u32_e32 v81, 0x40000, v1
	v_add_u32_e32 v82, 0x80000, v1
	v_add_u32_e32 v83, 0xc0000, v1
	v_add_u32_e32 v84, 0x100000, v1
	v_add_u32_e32 v85, 0x140000, v1
	v_add_u32_e32 v86, 0x180000, v1
	v_add_u32_e32 v87, 0x1c0000, v1
	v_add_u32_e32 v88, 0x200000, v1
	v_add_u32_e32 v89, 0x240000, v1
	v_add_u32_e32 v90, 0x280000, v1
	v_add_u32_e32 v91, 0x2c0000, v1
	v_add_u32_e32 v92, 0x300000, v1
	v_add_u32_e32 v93, 0x340000, v1
	v_add_u32_e32 v94, 0x380000, v1
	v_add_u32_e32 v95, 0x3c0000, v1
	v_add_u32_e32 v96, 0x400000, v1
	v_add_u32_e32 v97, 0x440000, v1
	v_add_u32_e32 v98, 0x480000, v1
	v_add_u32_e32 v99, 0x4c0000, v1
	v_add_u32_e32 v100, 0x500000, v1
	v_add_u32_e32 v101, 0x540000, v1
	v_add_u32_e32 v102, 0x580000, v1
	v_add_u32_e32 v103, 0x5c0000, v1
	v_add_u32_e32 v104, 0x600000, v1
	v_add_u32_e32 v105, 0x640000, v1
	v_add_u32_e32 v106, 0x680000, v1
	v_add_u32_e32 v107, 0x6c0000, v1
	v_add_u32_e32 v108, 0x700000, v1
	v_add_u32_e32 v109, 0x740000, v1
	v_add_u32_e32 v110, 0x780000, v1
	v_add_u32_e32 v111, 0x7c0000, v1
	s_waitcnt lgkmcnt(0)
	global_load_dwordx2 v[10:11], v1, s[4:5] nt
	global_load_dwordx2 v[12:13], v81, s[4:5] nt
	global_load_dwordx2 v[14:15], v82, s[4:5] nt
	global_load_dwordx2 v[16:17], v83, s[4:5] nt
	global_load_dwordx2 v[18:19], v84, s[4:5] nt
	global_load_dwordx2 v[20:21], v85, s[4:5] nt
	global_load_dwordx2 v[22:23], v86, s[4:5] nt
	global_load_dwordx2 v[24:25], v87, s[4:5] nt
	global_load_dwordx2 v[26:27], v88, s[4:5] nt
	global_load_dwordx2 v[28:29], v89, s[4:5] nt
	global_load_dwordx2 v[30:31], v90, s[4:5] nt
	global_load_dwordx2 v[32:33], v91, s[4:5] nt
	global_load_dwordx2 v[34:35], v92, s[4:5] nt
	global_load_dwordx2 v[36:37], v93, s[4:5] nt
	global_load_dwordx2 v[38:39], v94, s[4:5] nt
	global_load_dwordx2 v[40:41], v95, s[4:5] nt
	global_load_dwordx2 v[42:43], v96, s[4:5] nt
	global_load_dwordx2 v[44:45], v97, s[4:5] nt
	global_load_dwordx2 v[46:47], v98, s[4:5] nt
	global_load_dwordx2 v[48:49], v99, s[4:5] nt
	global_load_dwordx2 v[50:51], v100, s[4:5] nt
	global_load_dwordx2 v[52:53], v101, s[4:5] nt
	global_load_dwordx2 v[54:55], v102, s[4:5] nt
	global_load_dwordx2 v[56:57], v103, s[4:5] nt
	global_load_dwordx2 v[58:59], v104, s[4:5] nt
	global_load_dwordx2 v[60:61], v105, s[4:5] nt
	global_load_dwordx2 v[62:63], v106, s[4:5] nt
	global_load_dwordx2 v[64:65], v107, s[4:5] nt
	global_load_dwordx2 v[66:67], v108, s[4:5] nt
	global_load_dwordx2 v[68:69], v109, s[4:5] nt
	global_load_dwordx2 v[70:71], v110, s[4:5] nt
	global_load_dwordx2 v[72:73], v111, s[4:5] nt
	s_waitcnt vmcnt(31)
	v_cvt_f32_f16_e32 v74, v10
	v_cvt_f32_f16_sdwa v75, v10 dst_sel:DWORD dst_unused:UNUSED_PAD src0_sel:WORD_1
	v_cvt_f32_f16_e32 v76, v11
	v_cvt_f32_f16_sdwa v77, v11 dst_sel:DWORD dst_unused:UNUSED_PAD src0_sel:WORD_1
	v_pk_add_f32 v[6:7], v[6:7], v[74:75]
	v_pk_add_f32 v[8:9], v[8:9], v[76:77]
	s_waitcnt vmcnt(30)
	v_cvt_f32_f16_e32 v74, v12
	v_cvt_f32_f16_sdwa v75, v12 dst_sel:DWORD dst_unused:UNUSED_PAD src0_sel:WORD_1
	v_cvt_f32_f16_e32 v76, v13
	v_cvt_f32_f16_sdwa v77, v13 dst_sel:DWORD dst_unused:UNUSED_PAD src0_sel:WORD_1
	v_pk_add_f32 v[6:7], v[6:7], v[74:75]
	v_pk_add_f32 v[8:9], v[8:9], v[76:77]
	s_waitcnt vmcnt(29)
	v_cvt_f32_f16_e32 v74, v14
	v_cvt_f32_f16_sdwa v75, v14 dst_sel:DWORD dst_unused:UNUSED_PAD src0_sel:WORD_1
	v_cvt_f32_f16_e32 v76, v15
	v_cvt_f32_f16_sdwa v77, v15 dst_sel:DWORD dst_unused:UNUSED_PAD src0_sel:WORD_1
	v_pk_add_f32 v[6:7], v[6:7], v[74:75]
	v_pk_add_f32 v[8:9], v[8:9], v[76:77]
	s_waitcnt vmcnt(28)
	v_cvt_f32_f16_e32 v74, v16
	v_cvt_f32_f16_sdwa v75, v16 dst_sel:DWORD dst_unused:UNUSED_PAD src0_sel:WORD_1
	v_cvt_f32_f16_e32 v76, v17
	v_cvt_f32_f16_sdwa v77, v17 dst_sel:DWORD dst_unused:UNUSED_PAD src0_sel:WORD_1
	v_pk_add_f32 v[6:7], v[6:7], v[74:75]
	v_pk_add_f32 v[8:9], v[8:9], v[76:77]
	s_waitcnt vmcnt(27)
	v_cvt_f32_f16_e32 v74, v18
	v_cvt_f32_f16_sdwa v75, v18 dst_sel:DWORD dst_unused:UNUSED_PAD src0_sel:WORD_1
	v_cvt_f32_f16_e32 v76, v19
	v_cvt_f32_f16_sdwa v77, v19 dst_sel:DWORD dst_unused:UNUSED_PAD src0_sel:WORD_1
	v_pk_add_f32 v[6:7], v[6:7], v[74:75]
	v_pk_add_f32 v[8:9], v[8:9], v[76:77]
	s_waitcnt vmcnt(26)
	v_cvt_f32_f16_e32 v74, v20
	v_cvt_f32_f16_sdwa v75, v20 dst_sel:DWORD dst_unused:UNUSED_PAD src0_sel:WORD_1
	v_cvt_f32_f16_e32 v76, v21
	v_cvt_f32_f16_sdwa v77, v21 dst_sel:DWORD dst_unused:UNUSED_PAD src0_sel:WORD_1
	v_pk_add_f32 v[6:7], v[6:7], v[74:75]
	v_pk_add_f32 v[8:9], v[8:9], v[76:77]
	s_waitcnt vmcnt(25)
	v_cvt_f32_f16_e32 v74, v22
	v_cvt_f32_f16_sdwa v75, v22 dst_sel:DWORD dst_unused:UNUSED_PAD src0_sel:WORD_1
	v_cvt_f32_f16_e32 v76, v23
	v_cvt_f32_f16_sdwa v77, v23 dst_sel:DWORD dst_unused:UNUSED_PAD src0_sel:WORD_1
	v_pk_add_f32 v[6:7], v[6:7], v[74:75]
	v_pk_add_f32 v[8:9], v[8:9], v[76:77]
	s_waitcnt vmcnt(24)
	v_cvt_f32_f16_e32 v74, v24
	v_cvt_f32_f16_sdwa v75, v24 dst_sel:DWORD dst_unused:UNUSED_PAD src0_sel:WORD_1
	v_cvt_f32_f16_e32 v76, v25
	v_cvt_f32_f16_sdwa v77, v25 dst_sel:DWORD dst_unused:UNUSED_PAD src0_sel:WORD_1
	v_pk_add_f32 v[6:7], v[6:7], v[74:75]
	v_pk_add_f32 v[8:9], v[8:9], v[76:77]
	s_waitcnt vmcnt(23)
	v_cvt_f32_f16_e32 v74, v26
	v_cvt_f32_f16_sdwa v75, v26 dst_sel:DWORD dst_unused:UNUSED_PAD src0_sel:WORD_1
	v_cvt_f32_f16_e32 v76, v27
	v_cvt_f32_f16_sdwa v77, v27 dst_sel:DWORD dst_unused:UNUSED_PAD src0_sel:WORD_1
	v_pk_add_f32 v[6:7], v[6:7], v[74:75]
	v_pk_add_f32 v[8:9], v[8:9], v[76:77]
	s_waitcnt vmcnt(22)
	v_cvt_f32_f16_e32 v74, v28
	v_cvt_f32_f16_sdwa v75, v28 dst_sel:DWORD dst_unused:UNUSED_PAD src0_sel:WORD_1
	v_cvt_f32_f16_e32 v76, v29
	v_cvt_f32_f16_sdwa v77, v29 dst_sel:DWORD dst_unused:UNUSED_PAD src0_sel:WORD_1
	v_pk_add_f32 v[6:7], v[6:7], v[74:75]
	v_pk_add_f32 v[8:9], v[8:9], v[76:77]
	s_waitcnt vmcnt(21)
	v_cvt_f32_f16_e32 v74, v30
	v_cvt_f32_f16_sdwa v75, v30 dst_sel:DWORD dst_unused:UNUSED_PAD src0_sel:WORD_1
	v_cvt_f32_f16_e32 v76, v31
	v_cvt_f32_f16_sdwa v77, v31 dst_sel:DWORD dst_unused:UNUSED_PAD src0_sel:WORD_1
	v_pk_add_f32 v[6:7], v[6:7], v[74:75]
	v_pk_add_f32 v[8:9], v[8:9], v[76:77]
	s_waitcnt vmcnt(20)
	v_cvt_f32_f16_e32 v74, v32
	v_cvt_f32_f16_sdwa v75, v32 dst_sel:DWORD dst_unused:UNUSED_PAD src0_sel:WORD_1
	v_cvt_f32_f16_e32 v76, v33
	v_cvt_f32_f16_sdwa v77, v33 dst_sel:DWORD dst_unused:UNUSED_PAD src0_sel:WORD_1
	v_pk_add_f32 v[6:7], v[6:7], v[74:75]
	v_pk_add_f32 v[8:9], v[8:9], v[76:77]
	s_waitcnt vmcnt(19)
	v_cvt_f32_f16_e32 v74, v34
	v_cvt_f32_f16_sdwa v75, v34 dst_sel:DWORD dst_unused:UNUSED_PAD src0_sel:WORD_1
	v_cvt_f32_f16_e32 v76, v35
	v_cvt_f32_f16_sdwa v77, v35 dst_sel:DWORD dst_unused:UNUSED_PAD src0_sel:WORD_1
	v_pk_add_f32 v[6:7], v[6:7], v[74:75]
	v_pk_add_f32 v[8:9], v[8:9], v[76:77]
	s_waitcnt vmcnt(18)
	v_cvt_f32_f16_e32 v74, v36
	v_cvt_f32_f16_sdwa v75, v36 dst_sel:DWORD dst_unused:UNUSED_PAD src0_sel:WORD_1
	v_cvt_f32_f16_e32 v76, v37
	v_cvt_f32_f16_sdwa v77, v37 dst_sel:DWORD dst_unused:UNUSED_PAD src0_sel:WORD_1
	v_pk_add_f32 v[6:7], v[6:7], v[74:75]
	v_pk_add_f32 v[8:9], v[8:9], v[76:77]
	s_waitcnt vmcnt(17)
	v_cvt_f32_f16_e32 v74, v38
	v_cvt_f32_f16_sdwa v75, v38 dst_sel:DWORD dst_unused:UNUSED_PAD src0_sel:WORD_1
	v_cvt_f32_f16_e32 v76, v39
	v_cvt_f32_f16_sdwa v77, v39 dst_sel:DWORD dst_unused:UNUSED_PAD src0_sel:WORD_1
	v_pk_add_f32 v[6:7], v[6:7], v[74:75]
	v_pk_add_f32 v[8:9], v[8:9], v[76:77]
	s_waitcnt vmcnt(16)
	v_cvt_f32_f16_e32 v74, v40
	v_cvt_f32_f16_sdwa v75, v40 dst_sel:DWORD dst_unused:UNUSED_PAD src0_sel:WORD_1
	v_cvt_f32_f16_e32 v76, v41
	v_cvt_f32_f16_sdwa v77, v41 dst_sel:DWORD dst_unused:UNUSED_PAD src0_sel:WORD_1
	v_pk_add_f32 v[6:7], v[6:7], v[74:75]
	v_pk_add_f32 v[8:9], v[8:9], v[76:77]
	s_waitcnt vmcnt(15)
	v_cvt_f32_f16_e32 v74, v42
	v_cvt_f32_f16_sdwa v75, v42 dst_sel:DWORD dst_unused:UNUSED_PAD src0_sel:WORD_1
	v_cvt_f32_f16_e32 v76, v43
	v_cvt_f32_f16_sdwa v77, v43 dst_sel:DWORD dst_unused:UNUSED_PAD src0_sel:WORD_1
	v_pk_add_f32 v[6:7], v[6:7], v[74:75]
	v_pk_add_f32 v[8:9], v[8:9], v[76:77]
	s_waitcnt vmcnt(14)
	v_cvt_f32_f16_e32 v74, v44
	v_cvt_f32_f16_sdwa v75, v44 dst_sel:DWORD dst_unused:UNUSED_PAD src0_sel:WORD_1
	v_cvt_f32_f16_e32 v76, v45
	v_cvt_f32_f16_sdwa v77, v45 dst_sel:DWORD dst_unused:UNUSED_PAD src0_sel:WORD_1
	v_pk_add_f32 v[6:7], v[6:7], v[74:75]
	v_pk_add_f32 v[8:9], v[8:9], v[76:77]
	s_waitcnt vmcnt(13)
	v_cvt_f32_f16_e32 v74, v46
	v_cvt_f32_f16_sdwa v75, v46 dst_sel:DWORD dst_unused:UNUSED_PAD src0_sel:WORD_1
	v_cvt_f32_f16_e32 v76, v47
	v_cvt_f32_f16_sdwa v77, v47 dst_sel:DWORD dst_unused:UNUSED_PAD src0_sel:WORD_1
	v_pk_add_f32 v[6:7], v[6:7], v[74:75]
	v_pk_add_f32 v[8:9], v[8:9], v[76:77]
	s_waitcnt vmcnt(12)
	v_cvt_f32_f16_e32 v74, v48
	v_cvt_f32_f16_sdwa v75, v48 dst_sel:DWORD dst_unused:UNUSED_PAD src0_sel:WORD_1
	v_cvt_f32_f16_e32 v76, v49
	v_cvt_f32_f16_sdwa v77, v49 dst_sel:DWORD dst_unused:UNUSED_PAD src0_sel:WORD_1
	v_pk_add_f32 v[6:7], v[6:7], v[74:75]
	v_pk_add_f32 v[8:9], v[8:9], v[76:77]
	s_waitcnt vmcnt(11)
	v_cvt_f32_f16_e32 v74, v50
	v_cvt_f32_f16_sdwa v75, v50 dst_sel:DWORD dst_unused:UNUSED_PAD src0_sel:WORD_1
	v_cvt_f32_f16_e32 v76, v51
	v_cvt_f32_f16_sdwa v77, v51 dst_sel:DWORD dst_unused:UNUSED_PAD src0_sel:WORD_1
	v_pk_add_f32 v[6:7], v[6:7], v[74:75]
	v_pk_add_f32 v[8:9], v[8:9], v[76:77]
	s_waitcnt vmcnt(10)
	v_cvt_f32_f16_e32 v74, v52
	v_cvt_f32_f16_sdwa v75, v52 dst_sel:DWORD dst_unused:UNUSED_PAD src0_sel:WORD_1
	v_cvt_f32_f16_e32 v76, v53
	v_cvt_f32_f16_sdwa v77, v53 dst_sel:DWORD dst_unused:UNUSED_PAD src0_sel:WORD_1
	v_pk_add_f32 v[6:7], v[6:7], v[74:75]
	v_pk_add_f32 v[8:9], v[8:9], v[76:77]
	s_waitcnt vmcnt(9)
	v_cvt_f32_f16_e32 v74, v54
	v_cvt_f32_f16_sdwa v75, v54 dst_sel:DWORD dst_unused:UNUSED_PAD src0_sel:WORD_1
	v_cvt_f32_f16_e32 v76, v55
	v_cvt_f32_f16_sdwa v77, v55 dst_sel:DWORD dst_unused:UNUSED_PAD src0_sel:WORD_1
	v_pk_add_f32 v[6:7], v[6:7], v[74:75]
	v_pk_add_f32 v[8:9], v[8:9], v[76:77]
	s_waitcnt vmcnt(8)
	v_cvt_f32_f16_e32 v74, v56
	v_cvt_f32_f16_sdwa v75, v56 dst_sel:DWORD dst_unused:UNUSED_PAD src0_sel:WORD_1
	v_cvt_f32_f16_e32 v76, v57
	v_cvt_f32_f16_sdwa v77, v57 dst_sel:DWORD dst_unused:UNUSED_PAD src0_sel:WORD_1
	v_pk_add_f32 v[6:7], v[6:7], v[74:75]
	v_pk_add_f32 v[8:9], v[8:9], v[76:77]
	s_waitcnt vmcnt(7)
	v_cvt_f32_f16_e32 v74, v58
	v_cvt_f32_f16_sdwa v75, v58 dst_sel:DWORD dst_unused:UNUSED_PAD src0_sel:WORD_1
	v_cvt_f32_f16_e32 v76, v59
	v_cvt_f32_f16_sdwa v77, v59 dst_sel:DWORD dst_unused:UNUSED_PAD src0_sel:WORD_1
	v_pk_add_f32 v[6:7], v[6:7], v[74:75]
	v_pk_add_f32 v[8:9], v[8:9], v[76:77]
	s_waitcnt vmcnt(6)
	v_cvt_f32_f16_e32 v74, v60
	v_cvt_f32_f16_sdwa v75, v60 dst_sel:DWORD dst_unused:UNUSED_PAD src0_sel:WORD_1
	v_cvt_f32_f16_e32 v76, v61
	v_cvt_f32_f16_sdwa v77, v61 dst_sel:DWORD dst_unused:UNUSED_PAD src0_sel:WORD_1
	v_pk_add_f32 v[6:7], v[6:7], v[74:75]
	v_pk_add_f32 v[8:9], v[8:9], v[76:77]
	s_waitcnt vmcnt(5)
	v_cvt_f32_f16_e32 v74, v62
	v_cvt_f32_f16_sdwa v75, v62 dst_sel:DWORD dst_unused:UNUSED_PAD src0_sel:WORD_1
	v_cvt_f32_f16_e32 v76, v63
	v_cvt_f32_f16_sdwa v77, v63 dst_sel:DWORD dst_unused:UNUSED_PAD src0_sel:WORD_1
	v_pk_add_f32 v[6:7], v[6:7], v[74:75]
	v_pk_add_f32 v[8:9], v[8:9], v[76:77]
	s_waitcnt vmcnt(4)
	v_cvt_f32_f16_e32 v74, v64
	v_cvt_f32_f16_sdwa v75, v64 dst_sel:DWORD dst_unused:UNUSED_PAD src0_sel:WORD_1
	v_cvt_f32_f16_e32 v76, v65
	v_cvt_f32_f16_sdwa v77, v65 dst_sel:DWORD dst_unused:UNUSED_PAD src0_sel:WORD_1
	v_pk_add_f32 v[6:7], v[6:7], v[74:75]
	v_pk_add_f32 v[8:9], v[8:9], v[76:77]
	s_waitcnt vmcnt(3)
	v_cvt_f32_f16_e32 v74, v66
	v_cvt_f32_f16_sdwa v75, v66 dst_sel:DWORD dst_unused:UNUSED_PAD src0_sel:WORD_1
	v_cvt_f32_f16_e32 v76, v67
	v_cvt_f32_f16_sdwa v77, v67 dst_sel:DWORD dst_unused:UNUSED_PAD src0_sel:WORD_1
	v_pk_add_f32 v[6:7], v[6:7], v[74:75]
	v_pk_add_f32 v[8:9], v[8:9], v[76:77]
	s_waitcnt vmcnt(2)
	v_cvt_f32_f16_e32 v74, v68
	v_cvt_f32_f16_sdwa v75, v68 dst_sel:DWORD dst_unused:UNUSED_PAD src0_sel:WORD_1
	v_cvt_f32_f16_e32 v76, v69
	v_cvt_f32_f16_sdwa v77, v69 dst_sel:DWORD dst_unused:UNUSED_PAD src0_sel:WORD_1
	v_pk_add_f32 v[6:7], v[6:7], v[74:75]
	v_pk_add_f32 v[8:9], v[8:9], v[76:77]
	s_waitcnt vmcnt(1)
	v_cvt_f32_f16_e32 v74, v70
	v_cvt_f32_f16_sdwa v75, v70 dst_sel:DWORD dst_unused:UNUSED_PAD src0_sel:WORD_1
	v_cvt_f32_f16_e32 v76, v71
	v_cvt_f32_f16_sdwa v77, v71 dst_sel:DWORD dst_unused:UNUSED_PAD src0_sel:WORD_1
	v_pk_add_f32 v[6:7], v[6:7], v[74:75]
	v_pk_add_f32 v[8:9], v[8:9], v[76:77]
	s_waitcnt vmcnt(0)
	v_cvt_f32_f16_e32 v74, v72
	v_cvt_f32_f16_sdwa v75, v72 dst_sel:DWORD dst_unused:UNUSED_PAD src0_sel:WORD_1
	v_cvt_f32_f16_e32 v76, v73
	v_cvt_f32_f16_sdwa v77, v73 dst_sel:DWORD dst_unused:UNUSED_PAD src0_sel:WORD_1
	v_pk_add_f32 v[6:7], v[6:7], v[74:75]
	v_pk_add_f32 v[8:9], v[8:9], v[76:77]
	v_lshlrev_b32_e32 v0, 2, v0
	v_ashrrev_i32_e32 v1, 4, v2
	v_and_b32_e32 v0, 28, v0
	s_movk_i32 s0, 0xffe0
	v_and_or_b32 v0, v1, s0, v0
	v_ashrrev_i32_e32 v1, 31, v0
	v_lshlrev_b64 v[0:1], 8, v[0:1]
	v_lshrrev_b32_e32 v2, 1, v2
	v_lshl_add_u64 v[0:1], s[6:7], 0, v[0:1]
	v_and_b32_e32 v2, 0xfc, v2
	v_mov_b32_e32 v3, 0
	v_lshl_add_u64 v[0:1], v[0:1], 0, v[2:3]
	v_mul_f32_e32 v2, 0x3b800000, v6
	global_store_dword v[0:1], v2, off
	v_mul_f32_e32 v2, 0x3b800000, v7
	global_store_dword v[0:1], v2, off offset:256
	v_mul_f32_e32 v2, 0x3b800000, v8
	global_store_dword v[0:1], v2, off offset:512
	v_mul_f32_e32 v2, 0x3b800000, v9
	global_store_dword v[0:1], v2, off offset:768
	s_endpgm

	.amdhsa_kernel _Z13reduce_kernelPKDF16_Pf
		.amdhsa_group_segment_fixed_size 0
		.amdhsa_private_segment_fixed_size 0
		.amdhsa_kernarg_size 16
		.amdhsa_user_sgpr_count 2
		.amdhsa_user_sgpr_dispatch_ptr 0
		.amdhsa_user_sgpr_queue_ptr 0
		.amdhsa_user_sgpr_kernarg_segment_ptr 1
		.amdhsa_user_sgpr_dispatch_id 0
		.amdhsa_user_sgpr_kernarg_preload_length 0
		.amdhsa_user_sgpr_kernarg_preload_offset 0
		.amdhsa_user_sgpr_private_segment_size 0
		.amdhsa_uses_dynamic_stack 0
		.amdhsa_enable_private_segment 0
		.amdhsa_system_sgpr_workgroup_id_x 1
		.amdhsa_system_sgpr_workgroup_id_y 0
		.amdhsa_system_sgpr_workgroup_id_z 0
		.amdhsa_system_sgpr_workgroup_info 0
		.amdhsa_system_vgpr_workitem_id 0
		.amdhsa_next_free_vgpr 112
		.amdhsa_next_free_sgpr 19
		.amdhsa_accum_offset 112
		.amdhsa_reserve_vcc 1
		.amdhsa_float_round_mode_32 0
		.amdhsa_float_round_mode_16_64 0
		.amdhsa_float_denorm_mode_32 3
		.amdhsa_float_denorm_mode_16_64 3
		.amdhsa_dx10_clamp 1
		.amdhsa_ieee_mode 1
		.amdhsa_fp16_overflow 0
		.amdhsa_tg_split 0
		.amdhsa_exception_fp_ieee_invalid_op 0
		.amdhsa_exception_fp_denorm_src 0
		.amdhsa_exception_fp_ieee_div_zero 0
		.amdhsa_exception_fp_ieee_overflow 0
		.amdhsa_exception_fp_ieee_underflow 0
		.amdhsa_exception_fp_ieee_inexact 0
		.amdhsa_exception_int_div_zero 0
	.end_amdhsa_kernel

amdhsa.kernels:
  - .agpr_count:     0
    .args:
      - .actual_access:  read_only
        .address_space:  global
        .offset:         0
        .size:           8
        .value_kind:     global_buffer
      - .actual_access:  read_only
        .address_space:  global
        .offset:         8
        .size:           8
        .value_kind:     global_buffer
      - .actual_access:  write_only
        .address_space:  global
        .offset:         16
        .size:           8
        .value_kind:     global_buffer
      - .actual_access:  read_only
        .address_space:  global
        .offset:         24
        .size:           8
        .value_kind:     global_buffer
      - .actual_access:  write_only
        .address_space:  global
        .offset:         32
        .size:           8
        .value_kind:     global_buffer
    .group_segment_fixed_size: 43008
    .kernarg_segment_align: 8
    .kernarg_segment_size: 40
    .language:       OpenCL C
    .language_version:
      - 2
      - 0
    .max_flat_workgroup_size: 256
    .name:           _Z15sim_prep_kernelPKfS0_PDF16_S0_S1_
    .private_segment_fixed_size: 0
    .sgpr_count:     43
    .sgpr_spill_count: 0
    .symbol:         _Z15sim_prep_kernelPKfS0_PDF16_S0_S1_.kd
    .uniform_work_group_size: 1
    .uses_dynamic_stack: false
    .vgpr_count:     129
    .vgpr_spill_count: 0
    .wavefront_size: 64
  - .agpr_count:     0
    .args:
      - .address_space:  global
        .offset:         0
        .size:           8
        .value_kind:     global_buffer
      - .address_space:  global
        .offset:         8
        .size:           8
        .value_kind:     global_buffer
      - .actual_access:  write_only
        .address_space:  global
        .offset:         16
        .size:           8
        .value_kind:     global_buffer
    .group_segment_fixed_size: 114688
    .kernarg_segment_align: 8
    .kernarg_segment_size: 24
    .language:       OpenCL C
    .language_version:
      - 2
      - 0
    .max_flat_workgroup_size: 512
    .name:           _Z9feat_gemmPKDF16_S0_PDF16_
    .private_segment_fixed_size: 0
    .sgpr_count:     53
    .sgpr_spill_count: 0
    .symbol:         _Z9feat_gemmPKDF16_S0_PDF16_.kd
    .uniform_work_group_size: 1
    .uses_dynamic_stack: false
    .vgpr_count:     192
    .vgpr_spill_count: 0
    .wavefront_size: 64
  - .agpr_count:     0
    .args:
      - .actual_access:  read_only
        .address_space:  global
        .offset:         0
        .size:           8
        .value_kind:     global_buffer
      - .actual_access:  write_only
        .address_space:  global
        .offset:         8
        .size:           8
        .value_kind:     global_buffer
    .group_segment_fixed_size: 0
    .kernarg_segment_align: 8
    .kernarg_segment_size: 16
    .language:       OpenCL C
    .language_version:
      - 2
      - 0
    .max_flat_workgroup_size: 256
    .name:           _Z13reduce_kernelPKDF16_Pf
    .private_segment_fixed_size: 0
    .sgpr_count:     25
    .sgpr_spill_count: 0
    .symbol:         _Z13reduce_kernelPKDF16_Pf.kd
    .uniform_work_group_size: 1
    .uses_dynamic_stack: false
    .vgpr_count:     112
    .vgpr_spill_count: 0
    .wavefront_size: 64
